# speedup vs baseline: 1.0098x; 1.0098x over previous
_Z12local_kernelPKfPKDF16_S2_Pf5HeadPS3_:
	s_load_dwordx2 s[4:5], s[0:1], 0x10
	s_load_dwordx4 s[40:43], s[0:1], 0x0
	s_load_dwordx2 s[6:7], s[0:1], 0x20
	s_load_dwordx8 s[24:31], s[0:1], 0x30
	s_load_dwordx4 s[36:39], s[0:1], 0x60
	v_bfe_u32 v1, v0, 6, 1
	v_and_b32_e32 v215, 63, v0
	v_and_b32_e32 v212, 31, v0
	v_lshrrev_b32_e32 v213, 6, v0
	v_mul_u32_u24_e32 v2, 0x94c0, v1
	v_lshrrev_b32_e32 v51, 5, v215
	v_lshlrev_b32_e32 v38, 1, v2
	v_mov_b32_e32 v39, 0
	v_lshlrev_b32_e32 v210, 4, v215
	v_mov_b32_e32 v211, 0
	v_lshlrev_b32_e32 v6, 1, v212
	v_mov_b32_e32 v7, 0
	v_lshlrev_b32_e32 v208, 4, v51
	v_mov_b32_e32 v209, 0
	v_lshlrev_b32_e32 v214, 3, v51
	v_lshl_or_b32 v22, s2, 3, v213
	v_mul_lo_u16_e32 v23, 52, v212
	v_lshrrev_b16_e32 v34, 8, v23
	v_ashrrev_i32_e32 v52, 1, v22
	s_movk_i32 s0, 0x3ff
	v_mad_u32_u24 v34, v34, s0, v52
	v_lshl_add_u32 v34, v34, 2, v34
	v_add_lshl_u32 v34, v34, v212, 6
	v_ashrrev_i32_e32 v35, 31, v34
	v_lshlrev_b32_e32 v217, 7, v52
	v_or_b32_e32 v52, v217, v215
	v_ashrrev_i32_e32 v53, 31, v52
	v_mul_u32_u24_e32 v50, 0x4540, v213
	v_cmp_gt_u32_e32 vcc, 20, v212
	s_waitcnt lgkmcnt(0)
	v_lshl_add_u64 v[40:41], s[4:5], 0, v[38:39]
	v_lshl_add_u64 v[34:35], v[34:35], 1, s[42:43]
	v_lshl_add_u64 v[52:53], v[52:53], 2, s[40:41]
	v_cmp_gt_u32_e64 s[4:5], 32, v215
	v_lshl_add_u64 v[46:47], v[40:41], 0, v[210:211]
	v_lshl_add_u64 v[44:45], v[40:41], 0, v[6:7]
	v_lshl_add_u64 v[48:49], v[34:35], 0, v[208:209]
	s_mov_b64 s[8:9], 0x7000
	v_lshl_add_u64 v[44:45], v[44:45], 0, s[8:9]
	v_mov_b32_e32 v38, 0
	v_mov_b32_e32 v72, 0
	v_mov_b32_e32 v73, 0
	s_and_saveexec_b64 s[10:11], s[4:5]
	global_load_ushort v72, v[44:45], off offset:1152
	global_load_ushort v73, v[44:45], off offset:1216
	global_load_ushort v38, v[44:45], off offset:1024
	global_load_ushort v39, v[44:45], off offset:1088
	s_mov_b64 exec, s[10:11]
	v_mov_b32_e32 v56, 0
	v_mov_b32_e32 v57, 0
	v_mov_b32_e32 v58, 0
	v_mov_b32_e32 v59, 0
	v_mov_b32_e32 v60, 0
	v_mov_b32_e32 v61, 0
	v_mov_b32_e32 v62, 0
	v_mov_b32_e32 v63, 0
	v_mov_b32_e32 v64, 0
	v_mov_b32_e32 v65, 0
	v_mov_b32_e32 v66, 0
	v_mov_b32_e32 v67, 0
	v_mov_b32_e32 v68, 0
	v_mov_b32_e32 v69, 0
	v_mov_b32_e32 v70, 0
	v_mov_b32_e32 v71, 0
	s_and_saveexec_b64 s[10:11], vcc
	global_load_dwordx4 v[56:59], v[48:49], off
	global_load_dwordx4 v[60:63], v[48:49], off offset:32
	global_load_dwordx4 v[64:67], v[48:49], off offset:64
	global_load_dwordx4 v[68:71], v[48:49], off offset:96
	s_mov_b64 exec, s[10:11]
	s_mov_b64 s[8:9], 0x7500
	v_lshl_add_u64 v[42:43], v[46:47], 0, s[8:9]
	global_load_dwordx4 v[220:223], v[42:43], off
	global_load_dwordx4 v[224:227], v[42:43], off offset:1024
	global_load_dwordx4 v[228:231], v[42:43], off offset:2048
	global_load_dwordx4 v[232:235], v[42:43], off offset:3072
	s_mov_b64 s[8:9], 0x8500
	v_lshl_add_u64 v[42:43], v[46:47], 0, s[8:9]
	global_load_dwordx4 v[236:239], v[42:43], off
	global_load_dwordx4 v[240:243], v[42:43], off offset:1024
	global_load_dwordx4 v[244:247], v[42:43], off offset:2048
	global_load_dwordx4 v[248:251], v[42:43], off offset:3072
	global_load_dword v218, v[52:53], off
	global_load_dword v219, v[52:53], off offset:256
	s_mov_b64 s[8:9], 0x7000
	v_lshl_add_u64 v[42:43], v[46:47], 0, s[8:9]
	global_load_dwordx4 v[200:203], v[42:43], off
	global_load_dwordx4 v[84:87], v[46:47], off
	global_load_dwordx4 v[88:91], v[46:47], off offset:1024
	global_load_dwordx4 v[92:95], v[46:47], off offset:2048
	global_load_dwordx4 v[100:103], v[46:47], off offset:3072
	s_mov_b64 s[8:9], 0x1000
	v_lshl_add_u64 v[42:43], v[46:47], 0, s[8:9]
	global_load_dwordx4 v[104:107], v[42:43], off
	global_load_dwordx4 v[108:111], v[42:43], off offset:1024
	global_load_dwordx4 v[112:115], v[42:43], off offset:2048
	global_load_dwordx4 v[116:119], v[42:43], off offset:3072
	s_mov_b64 s[8:9], 0x2000
	v_lshl_add_u64 v[42:43], v[46:47], 0, s[8:9]
	global_load_dwordx4 v[128:131], v[42:43], off
	global_load_dwordx4 v[120:123], v[42:43], off offset:1024
	global_load_dwordx4 v[124:127], v[42:43], off offset:2048
	global_load_dwordx4 v[152:155], v[42:43], off offset:3072
	s_mov_b64 s[8:9], 0x3000
	v_lshl_add_u64 v[42:43], v[46:47], 0, s[8:9]
	global_load_dwordx4 v[132:135], v[42:43], off
	global_load_dwordx4 v[136:139], v[42:43], off offset:1024
	global_load_dwordx4 v[140:143], v[42:43], off offset:2048
	global_load_dwordx4 v[144:147], v[42:43], off offset:3072
	s_mov_b64 s[8:9], 0x4000
	v_lshl_add_u64 v[42:43], v[46:47], 0, s[8:9]
	global_load_dwordx4 v[148:151], v[42:43], off
	global_load_dwordx4 v[156:159], v[42:43], off offset:1024
	global_load_dwordx4 v[160:163], v[42:43], off offset:2048
	global_load_dwordx4 v[164:167], v[42:43], off offset:3072
	s_mov_b64 s[8:9], 0x5000
	v_lshl_add_u64 v[42:43], v[46:47], 0, s[8:9]
	global_load_dwordx4 v[168:171], v[42:43], off
	global_load_dwordx4 v[172:175], v[42:43], off offset:1024
	global_load_dwordx4 v[176:179], v[42:43], off offset:2048
	global_load_dwordx4 v[180:183], v[42:43], off offset:3072
	s_mov_b64 s[8:9], 0x6000
	v_lshl_add_u64 v[42:43], v[46:47], 0, s[8:9]
	global_load_dwordx4 v[184:187], v[42:43], off
	global_load_dwordx4 v[188:191], v[42:43], off offset:1024
	global_load_dwordx4 v[192:195], v[42:43], off offset:2048
	global_load_dwordx4 v[196:199], v[42:43], off offset:3072
	v_mov_b32_e32 v74, 0
	v_mov_b32_e32 v75, 0
	v_mov_b32_e32 v76, 0
	v_mov_b32_e32 v77, 0
	v_or_b32_e32 v78, 0xffffffc0, v215
	v_add_u32_e32 v79, v50, v210
	v_add_u32_e32 v211, v50, v210
	s_mov_b64 s[0:1], 0
	s_movk_i32 s3, 0x413
.Lpro_zero:
	v_add_u32_e32 v78, 64, v78
	v_cmp_lt_u32_e32 vcc, s3, v78
	ds_write_b128 v79, v[74:77]
	s_or_b64 s[0:1], vcc, s[0:1]
	v_add_u32_e32 v79, 0x400, v79
	s_andn2_b64 exec, exec, s[0:1]
	s_cbranch_execnz .Lpro_zero
	s_or_b64 exec, exec, s[0:1]
	v_mov_b32_e32 v3, 0x3c00
	v_cndmask_b32_e64 v3, 0, v3, s[4:5]
	v_pack_b32_f16 v96, v3, 0
	v_mov_b32_e32 v97, 0
	v_mov_b32_e32 v98, 0
	v_mov_b32_e32 v99, 0
	v_mov_b32_e32 v77, 0
	v_mov_b32_e32 v78, 0
	v_mov_b32_e32 v79, 0
	v_mov_b32_e32 v53, 0
	v_mov_b32_e32 v54, 0
	v_mov_b32_e32 v55, 0
	s_waitcnt vmcnt(43)
	v_and_b32_e32 v76, 0xffff, v72
	v_and_b32_e32 v52, 0xffff, v73
	s_nop 1
	v_mfma_f32_32x32x16_f16 v[2:17], v[76:79], v[96:99], 0
	v_mfma_f32_32x32x16_f16 v[18:33], v[52:55], v[96:99], 0
	s_waitcnt vmcnt(31)
	v_mfma_f32_32x32x16_f16 v[2:17], v[220:223], v[56:59], v[2:17]
	v_mfma_f32_32x32x16_f16 v[18:33], v[224:227], v[56:59], v[18:33]
	v_mfma_f32_32x32x16_f16 v[2:17], v[228:231], v[60:63], v[2:17]
	v_mfma_f32_32x32x16_f16 v[18:33], v[232:235], v[60:63], v[18:33]
	v_mfma_f32_32x32x16_f16 v[2:17], v[236:239], v[64:67], v[2:17]
	v_mfma_f32_32x32x16_f16 v[18:33], v[240:243], v[64:67], v[18:33]
	v_mfma_f32_32x32x16_f16 v[2:17], v[244:247], v[68:71], v[2:17]
	v_mfma_f32_32x32x16_f16 v[18:33], v[248:251], v[68:71], v[18:33]
	v_readfirstlane_b32 s0, v0
	s_mov_b32 s3, 0
	s_nop 11
	v_cvt_pk_f16_f32 v9, v8, v9
	v_cvt_pk_f16_f32 v8, v6, v7
	v_cvt_pk_f16_f32 v7, v4, v5
	v_cvt_pk_f16_f32 v6, v2, v3
	v_cvt_pk_f16_f32 v5, v24, v25
	v_cvt_pk_f16_f32 v4, v22, v23
	v_cvt_pk_f16_f32 v3, v20, v21
	v_cvt_pk_f16_f32 v2, v18, v19
	v_cvt_pk_f16_f32 v17, v16, v17
	v_cvt_pk_f16_f32 v16, v14, v15
	v_cvt_pk_f16_f32 v15, v12, v13
	v_cvt_pk_f16_f32 v14, v10, v11
	v_cvt_pk_f16_f32 v11, v32, v33
	v_cvt_pk_f16_f32 v10, v30, v31
	ds_write_b128 v211, v[6:9] offset:13632
	ds_write_b128 v211, v[2:5] offset:15680
	ds_write_b128 v211, v[14:17] offset:14656
	v_cvt_pk_f16_f32 v9, v28, v29
	v_cvt_pk_f16_f32 v8, v26, v27
	ds_write_b128 v211, v[8:11] offset:16704
	s_cmpk_lt_i32 s0, 0x100
	s_cbranch_scc1 .LBB0_20
	s_setprio 1
.LBB0_20:
	v_mov_b32_e32 v81, 0
	v_lshlrev_b32_e32 v4, 3, v0
	v_lshrrev_b32_e32 v2, 2, v0
	v_lshlrev_b32_e32 v3, 1, v0
	v_bfe_i32 v5, v0, 0, 1
	v_lshrrev_b32_e32 v0, 5, v0
	v_and_b32_e32 v5, 0x120, v5
	v_and_b32_e32 v221, 12, v0
	v_add_u16_e32 v0, v214, v212
	v_add_u32_e32 v5, v50, v5
	v_mul_u32_u24_e32 v1, 0x2800, v1
	v_lshrrev_b16_e32 v0, 1, v0
	v_or_b32_e32 v1, v1, v214
	v_lshl_add_u32 v223, v0, 2, v5
	v_add_lshl_u32 v0, v214, v212, 1
	v_lshlrev_b32_e32 v216, 2, v51
	s_movk_i32 s0, 0x88
	v_add_u32_e32 v222, 0x22a00, v1
	v_add_u32_e32 v1, 64, v0
	v_add_u32_e32 v0, 0xc0, v0
	v_and_or_b32 v2, v2, 3, v216
	v_lshlrev_b32_e32 v6, 4, v212
	v_mad_u32_u24 v8, v212, s0, v50
	v_and_b32_e32 v0, 0x1fc, v0
	s_movk_i32 s0, 0x880
	v_mul_u32_u24_e32 v2, 0x88, v2
	v_and_b32_e32 v3, 32, v3
	v_add_u32_e32 v7, v50, v6
	v_add_u32_e32 v225, v5, v0
	v_mad_u32_u24 v0, v51, s0, v50
	s_movk_i32 s0, 0x240
	v_and_b32_e32 v4, 24, v4
	v_add3_u32 v2, v50, v2, v3
	v_and_b32_e32 v1, 0xfc, v1
	v_add3_u32 v226, v0, v6, s0
	v_add_u32_e32 v228, v7, v214
	v_mbcnt_lo_u32_b32 v0, -1, 0
	v_and_b32_e32 v80, 0xffff, v39
	v_mov_b32_e32 v82, v81
	v_mov_b32_e32 v83, v81
	v_and_b32_e32 v204, 0xffff, v38
	v_mov_b32_e32 v205, v81
	v_mov_b32_e32 v206, v81
	v_mov_b32_e32 v207, v81
	v_lshl_add_u32 v220, v215, 1, v50
	v_add_u32_e32 v224, v5, v1
	s_brev_b32 s33, 61
	s_brev_b32 s34, 60
	s_mov_b32 s35, 0x7fff7fff
	s_mov_b32 s42, 0xa714a714
	v_mov_b32_e32 v227, 0xb7d0b7d0
	s_mov_b32 s43, 0xbc90bc90
	v_add_u32_e32 v229, v8, v214
	v_add_u32_e32 v230, v2, v4
	v_add_u32_e32 v231, 0xf0, v228
	v_add_u32_e32 v232, 0x170, v228
	v_add_u32_e32 v233, 0x1f0, v228
	v_add_u32_e32 v234, 0x70, v228
	v_mbcnt_hi_u32_b32 v235, -1, v0
	s_waitcnt vmcnt(28)
	s_branch .LBB0_22
.LBB0_21:
	s_or_b64 exec, exec, s[0:1]
	s_waitcnt vmcnt(0)
	s_add_i32 s3, s3, 1
	s_cmp_eq_u32 s3, 4
	s_cbranch_scc1 .LBB0_30
.LBB0_22:
	s_cmp_eq_u32 s3, 3
	v_lshl_add_u32 v0, s3, 17, v217
	v_add_u32_e32 v1, 0x20000, v0
	s_cselect_b64 vcc, -1, 0
	v_cndmask_b32_e32 v0, v1, v0, vcc
	v_or_b32_e32 v0, v0, v215
	v_ashrrev_i32_e32 v1, 31, v0
	v_lshl_add_u64 v[0:1], v[0:1], 2, s[40:41]
	v_mov_b32_e32 v2, v219
	v_mov_b32_e32 v3, v218
	global_load_dword v218, v[0:1], off
	global_load_dword v219, v[0:1], off offset:256
	v_add_f32_e32 v0, v2, v3
	s_nop 1
	v_add_f32_dpp v0, v0, v0 quad_perm:[1,0,3,2] row_mask:0xf bank_mask:0xf bound_ctrl:1
	s_nop 1
	v_add_f32_dpp v0, v0, v0 quad_perm:[2,3,0,1] row_mask:0xf bank_mask:0xf bound_ctrl:1
	s_nop 1
	v_add_f32_dpp v0, v0, v0 row_half_mirror row_mask:0xf bank_mask:0xf bound_ctrl:1
	s_nop 1
	v_add_f32_dpp v0, v0, v0 row_mirror row_mask:0xf bank_mask:0xf bound_ctrl:1
	s_nop 0
	v_readlane_b32 s1, v0, 16
	v_readlane_b32 s9, v0, 48
	v_readlane_b32 s0, v0, 0
	v_readlane_b32 s8, v0, 32
	v_mov_b32_e32 v0, s1
	v_mov_b32_e32 v1, s9
	v_add_f32_e32 v0, s0, v0
	v_add_f32_e32 v1, s8, v1
	v_add_f32_e32 v0, v0, v1
	v_fma_mixlo_f16 v1, v0, s33, v3
	v_fma_mixlo_f16 v0, v0, s33, v2
	ds_write_b16 v220, v1 offset:14
	ds_write_b16 v220, v0 offset:142
	ds_write_b16 v220, v1 offset:300
	ds_write_b16 v220, v0 offset:428
	ds_read2_b32 v[2:3], v223 offset0:2 offset1:3
	ds_read2_b32 v[0:1], v223 offset1:1
	ds_read2_b32 v[4:5], v223 offset0:32 offset1:33
	ds_read2_b32 v[6:7], v223 offset0:34 offset1:35
	s_mov_b32 s8, 0
	s_mov_b32 s9, s8
	s_mov_b32 s10, s8
	s_waitcnt lgkmcnt(3)
	v_or_b32_sdwa v8, v3, s34 dst_sel:DWORD dst_unused:UNUSED_PAD src0_sel:WORD_0 src1_sel:DWORD
	v_cndmask_b32_e64 v3, v8, v3, s[4:5]
	s_mov_b32 s11, s8
	s_mov_b32 s12, s8
	s_waitcnt lgkmcnt(2)
	v_mfma_f32_32x32x16_f16 v[64:79], v[200:203], v[0:3], 0
	ds_read2_b32 v[2:3], v224 offset0:2 offset1:3
	ds_read2_b32 v[0:1], v224 offset1:1
	ds_read2_b32 v[16:17], v225 offset1:1
	ds_read2_b32 v[18:19], v225 offset0:2 offset1:3
	s_mov_b32 s13, s8
	s_mov_b32 s14, s8
	s_mov_b32 s15, s8
	s_waitcnt lgkmcnt(3)
	v_or_b32_sdwa v8, v3, s34 dst_sel:DWORD dst_unused:UNUSED_PAD src0_sel:WORD_0 src1_sel:DWORD
	s_waitcnt lgkmcnt(0)
	v_or_b32_sdwa v20, v19, s34 dst_sel:DWORD dst_unused:UNUSED_PAD src0_sel:WORD_0 src1_sel:DWORD
	v_cndmask_b32_e64 v19, v20, v19, s[4:5]
	v_cndmask_b32_e64 v3, v8, v3, s[4:5]
	s_mov_b32 s16, s8
	v_mfma_f32_32x32x16_f16 v[16:31], v[200:203], v[16:19], 0
	s_mov_b32 s17, s8
	s_mov_b32 s18, s8
	s_mov_b32 s19, s8
	s_mov_b32 s20, s8
	s_mov_b32 s21, s8
	s_mov_b32 s22, s8
	s_mov_b32 s23, s8
	v_mfma_f32_32x32x16_f16 v[48:63], v[200:203], v[0:3], 0
	v_or_b32_sdwa v0, v7, s34 dst_sel:DWORD dst_unused:UNUSED_PAD src0_sel:WORD_0 src1_sel:DWORD
	v_cndmask_b32_e64 v7, v0, v7, s[4:5]
	s_nop 1
	v_mfma_f32_32x32x16_f16 v[32:47], v[200:203], v[4:7], 0
	v_mov_b64_e32 v[0:1], s[8:9]
	v_mov_b64_e32 v[2:3], s[10:11]
	v_mov_b64_e32 v[4:5], s[12:13]
	v_mov_b64_e32 v[6:7], s[14:15]
	v_mov_b64_e32 v[8:9], s[16:17]
	v_mov_b64_e32 v[10:11], s[18:19]
	v_mov_b64_e32 v[12:13], s[20:21]
	v_mov_b64_e32 v[14:15], s[22:23]
	s_nop 15
	s_nop 3
	v_cvt_pk_f16_f32 v239, v64, v65
	v_cvt_pk_f16_f32 v240, v66, v67
	v_and_b32 v209, s35, v239
	v_and_b32 v238, s35, v240
	v_pk_fma_f16 v236, v209, s42, v227
	v_pk_fma_f16 v237, v238, s42, v227
	v_pk_fma_f16 v236, v236, v209, s43
	v_pk_fma_f16 v237, v237, v238, s43
	s_nop 0
	v_pk_mul_f16 v236, v236, v209
	v_pk_mul_f16 v237, v237, v238
	v_exp_f16_sdwa v236, v236 dst_sel:WORD_0 dst_unused:UNUSED_PRESERVE src0_sel:WORD_0
	v_exp_f16_sdwa v237, v237 dst_sel:WORD_0 dst_unused:UNUSED_PRESERVE src0_sel:WORD_0
	v_exp_f16_sdwa v236, v236 dst_sel:WORD_1 dst_unused:UNUSED_PRESERVE src0_sel:WORD_1
	v_exp_f16_sdwa v237, v237 dst_sel:WORD_1 dst_unused:UNUSED_PRESERVE src0_sel:WORD_1
	v_pk_add_f16 v64, v239, v209
	v_pk_add_f16 v65, v240, v238
	v_pk_fma_f16 v236, v209, v236, v64 neg_lo:[1,0,0] neg_hi:[1,0,0]
	v_pk_fma_f16 v237, v238, v237, v65 neg_lo:[1,0,0] neg_hi:[1,0,0]
	s_nop 0
	v_cvt_pk_f16_f32 v209, v68, v69
	v_cvt_pk_f16_f32 v238, v70, v71
	v_and_b32 v66, s35, v209
	v_and_b32 v67, s35, v238
	v_pk_fma_f16 v64, v66, s42, v227
	v_pk_fma_f16 v65, v67, s42, v227
	v_pk_fma_f16 v64, v64, v66, s43
	v_pk_fma_f16 v65, v65, v67, s43
	s_nop 0
	v_pk_mul_f16 v64, v64, v66
	v_pk_mul_f16 v65, v65, v67
	v_exp_f16_sdwa v64, v64 dst_sel:WORD_0 dst_unused:UNUSED_PRESERVE src0_sel:WORD_0
	v_exp_f16_sdwa v65, v65 dst_sel:WORD_0 dst_unused:UNUSED_PRESERVE src0_sel:WORD_0
	v_exp_f16_sdwa v64, v64 dst_sel:WORD_1 dst_unused:UNUSED_PRESERVE src0_sel:WORD_1
	v_exp_f16_sdwa v65, v65 dst_sel:WORD_1 dst_unused:UNUSED_PRESERVE src0_sel:WORD_1
	v_pk_add_f16 v68, v209, v66
	v_pk_add_f16 v69, v238, v67
	v_pk_fma_f16 v64, v66, v64, v68 neg_lo:[1,0,0] neg_hi:[1,0,0]
	v_pk_fma_f16 v65, v67, v65, v69 neg_lo:[1,0,0] neg_hi:[1,0,0]
	s_nop 0
	v_cvt_pk_f16_f32 v70, v72, v73
	v_cvt_pk_f16_f32 v71, v74, v75
	v_and_b32 v68, s35, v70
	v_and_b32 v69, s35, v71
	v_pk_fma_f16 v66, v68, s42, v227
	v_pk_fma_f16 v67, v69, s42, v227
	v_pk_fma_f16 v66, v66, v68, s43
	v_pk_fma_f16 v67, v67, v69, s43
	s_nop 0
	v_pk_mul_f16 v66, v66, v68
	v_pk_mul_f16 v67, v67, v69
	v_exp_f16_sdwa v66, v66 dst_sel:WORD_0 dst_unused:UNUSED_PRESERVE src0_sel:WORD_0
	v_exp_f16_sdwa v67, v67 dst_sel:WORD_0 dst_unused:UNUSED_PRESERVE src0_sel:WORD_0
	v_exp_f16_sdwa v66, v66 dst_sel:WORD_1 dst_unused:UNUSED_PRESERVE src0_sel:WORD_1
	v_exp_f16_sdwa v67, v67 dst_sel:WORD_1 dst_unused:UNUSED_PRESERVE src0_sel:WORD_1
	v_pk_add_f16 v72, v70, v68
	v_pk_add_f16 v73, v71, v69
	v_pk_fma_f16 v66, v68, v66, v72 neg_lo:[1,0,0] neg_hi:[1,0,0]
	v_pk_fma_f16 v67, v69, v67, v73 neg_lo:[1,0,0] neg_hi:[1,0,0]
	s_nop 0
	v_cvt_pk_f16_f32 v72, v76, v77
	v_cvt_pk_f16_f32 v73, v78, v79
	v_and_b32 v70, s35, v72
	v_and_b32 v71, s35, v73
	v_pk_fma_f16 v68, v70, s42, v227
	v_pk_fma_f16 v69, v71, s42, v227
	v_pk_fma_f16 v68, v68, v70, s43
	v_pk_fma_f16 v69, v69, v71, s43
	s_nop 0
	v_pk_mul_f16 v68, v68, v70
	v_pk_mul_f16 v69, v69, v71
	v_exp_f16_sdwa v68, v68 dst_sel:WORD_0 dst_unused:UNUSED_PRESERVE src0_sel:WORD_0
	v_exp_f16_sdwa v69, v69 dst_sel:WORD_0 dst_unused:UNUSED_PRESERVE src0_sel:WORD_0
	v_exp_f16_sdwa v68, v68 dst_sel:WORD_1 dst_unused:UNUSED_PRESERVE src0_sel:WORD_1
	v_exp_f16_sdwa v69, v69 dst_sel:WORD_1 dst_unused:UNUSED_PRESERVE src0_sel:WORD_1
	v_pk_add_f16 v74, v72, v70
	v_pk_add_f16 v75, v73, v71
	v_pk_fma_f16 v68, v70, v68, v74 neg_lo:[1,0,0] neg_hi:[1,0,0]
	v_pk_fma_f16 v69, v71, v69, v75 neg_lo:[1,0,0] neg_hi:[1,0,0]
	s_nop 0
	v_cvt_pk_f16_f32 v74, v48, v49
	v_cvt_pk_f16_f32 v75, v50, v51
	v_and_b32 v72, s35, v74
	v_and_b32 v73, s35, v75
	v_pk_fma_f16 v70, v72, s42, v227
	v_pk_fma_f16 v71, v73, s42, v227
	v_pk_fma_f16 v70, v70, v72, s43
	v_pk_fma_f16 v71, v71, v73, s43
	s_nop 0
	v_pk_mul_f16 v70, v70, v72
	v_pk_mul_f16 v71, v71, v73
	v_exp_f16_sdwa v70, v70 dst_sel:WORD_0 dst_unused:UNUSED_PRESERVE src0_sel:WORD_0
	v_exp_f16_sdwa v71, v71 dst_sel:WORD_0 dst_unused:UNUSED_PRESERVE src0_sel:WORD_0
	v_exp_f16_sdwa v70, v70 dst_sel:WORD_1 dst_unused:UNUSED_PRESERVE src0_sel:WORD_1
	v_exp_f16_sdwa v71, v71 dst_sel:WORD_1 dst_unused:UNUSED_PRESERVE src0_sel:WORD_1
	v_pk_add_f16 v48, v74, v72
	v_pk_add_f16 v49, v75, v73
	v_pk_fma_f16 v70, v72, v70, v48 neg_lo:[1,0,0] neg_hi:[1,0,0]
	v_pk_fma_f16 v71, v73, v71, v49 neg_lo:[1,0,0] neg_hi:[1,0,0]
	s_nop 0
	v_cvt_pk_f16_f32 v72, v52, v53
	v_cvt_pk_f16_f32 v73, v54, v55
	v_and_b32 v50, s35, v72
	v_and_b32 v51, s35, v73
	v_pk_fma_f16 v48, v50, s42, v227
	v_pk_fma_f16 v49, v51, s42, v227
	v_pk_fma_f16 v48, v48, v50, s43
	v_pk_fma_f16 v49, v49, v51, s43
	s_nop 0
	v_pk_mul_f16 v48, v48, v50
	v_pk_mul_f16 v49, v49, v51
	v_exp_f16_sdwa v48, v48 dst_sel:WORD_0 dst_unused:UNUSED_PRESERVE src0_sel:WORD_0
	v_exp_f16_sdwa v49, v49 dst_sel:WORD_0 dst_unused:UNUSED_PRESERVE src0_sel:WORD_0
	v_exp_f16_sdwa v48, v48 dst_sel:WORD_1 dst_unused:UNUSED_PRESERVE src0_sel:WORD_1
	v_exp_f16_sdwa v49, v49 dst_sel:WORD_1 dst_unused:UNUSED_PRESERVE src0_sel:WORD_1
	v_pk_add_f16 v52, v72, v50
	v_pk_add_f16 v53, v73, v51
	v_pk_fma_f16 v48, v50, v48, v52 neg_lo:[1,0,0] neg_hi:[1,0,0]
	v_pk_fma_f16 v49, v51, v49, v53 neg_lo:[1,0,0] neg_hi:[1,0,0]
	s_nop 0
	v_cvt_pk_f16_f32 v54, v56, v57
	v_cvt_pk_f16_f32 v55, v58, v59
	v_and_b32 v52, s35, v54
	v_and_b32 v53, s35, v55
	v_pk_fma_f16 v50, v52, s42, v227
	v_pk_fma_f16 v51, v53, s42, v227
	v_pk_fma_f16 v50, v50, v52, s43
	v_pk_fma_f16 v51, v51, v53, s43
	s_nop 0
	v_pk_mul_f16 v50, v50, v52
	v_pk_mul_f16 v51, v51, v53
	v_exp_f16_sdwa v50, v50 dst_sel:WORD_0 dst_unused:UNUSED_PRESERVE src0_sel:WORD_0
	v_exp_f16_sdwa v51, v51 dst_sel:WORD_0 dst_unused:UNUSED_PRESERVE src0_sel:WORD_0
	v_exp_f16_sdwa v50, v50 dst_sel:WORD_1 dst_unused:UNUSED_PRESERVE src0_sel:WORD_1
	v_exp_f16_sdwa v51, v51 dst_sel:WORD_1 dst_unused:UNUSED_PRESERVE src0_sel:WORD_1
	v_pk_add_f16 v56, v54, v52
	v_pk_add_f16 v57, v55, v53
	v_pk_fma_f16 v50, v52, v50, v56 neg_lo:[1,0,0] neg_hi:[1,0,0]
	v_pk_fma_f16 v51, v53, v51, v57 neg_lo:[1,0,0] neg_hi:[1,0,0]
	s_nop 0
	v_cvt_pk_f16_f32 v56, v60, v61
	v_cvt_pk_f16_f32 v57, v62, v63
	v_and_b32 v54, s35, v56
	v_and_b32 v55, s35, v57
	v_pk_fma_f16 v52, v54, s42, v227
	v_pk_fma_f16 v53, v55, s42, v227
	v_pk_fma_f16 v52, v52, v54, s43
	v_pk_fma_f16 v53, v53, v55, s43
	s_nop 0
	v_pk_mul_f16 v52, v52, v54
	v_pk_mul_f16 v53, v53, v55
	v_exp_f16_sdwa v52, v52 dst_sel:WORD_0 dst_unused:UNUSED_PRESERVE src0_sel:WORD_0
	v_exp_f16_sdwa v53, v53 dst_sel:WORD_0 dst_unused:UNUSED_PRESERVE src0_sel:WORD_0
	v_exp_f16_sdwa v52, v52 dst_sel:WORD_1 dst_unused:UNUSED_PRESERVE src0_sel:WORD_1
	v_exp_f16_sdwa v53, v53 dst_sel:WORD_1 dst_unused:UNUSED_PRESERVE src0_sel:WORD_1
	v_pk_add_f16 v58, v56, v54
	v_pk_add_f16 v59, v57, v55
	v_pk_fma_f16 v52, v54, v52, v58 neg_lo:[1,0,0] neg_hi:[1,0,0]
	v_pk_fma_f16 v53, v55, v53, v59 neg_lo:[1,0,0] neg_hi:[1,0,0]
	ds_write2_b64 v228, v[236:237], v[70:71] offset0:78 offset1:142
	ds_write2st64_b64 v231, v[64:65], v[48:49] offset0:5 offset1:6
	ds_write2st64_b64 v232, v[66:67], v[50:51] offset0:9 offset1:10
	ds_write2st64_b64 v233, v[68:69], v[52:53] offset0:13 offset1:14
	v_cvt_pk_f16_f32 v52, v32, v33
	v_cvt_pk_f16_f32 v53, v34, v35
	v_and_b32 v50, s35, v52
	v_and_b32 v51, s35, v53
	v_pk_fma_f16 v48, v50, s42, v227
	v_pk_fma_f16 v49, v51, s42, v227
	v_pk_fma_f16 v48, v48, v50, s43
	v_pk_fma_f16 v49, v49, v51, s43
	v_mov_b32_e32 v237, 0xff800000
	v_pk_mul_f16 v48, v48, v50
	v_pk_mul_f16 v49, v49, v51
	v_exp_f16_sdwa v48, v48 dst_sel:WORD_0 dst_unused:UNUSED_PRESERVE src0_sel:WORD_0
	v_exp_f16_sdwa v49, v49 dst_sel:WORD_0 dst_unused:UNUSED_PRESERVE src0_sel:WORD_0
	v_exp_f16_sdwa v48, v48 dst_sel:WORD_1 dst_unused:UNUSED_PRESERVE src0_sel:WORD_1
	v_exp_f16_sdwa v49, v49 dst_sel:WORD_1 dst_unused:UNUSED_PRESERVE src0_sel:WORD_1
	v_pk_add_f16 v32, v52, v50
	v_pk_add_f16 v33, v53, v51
	v_pk_fma_f16 v48, v50, v48, v32 neg_lo:[1,0,0] neg_hi:[1,0,0]
	v_pk_fma_f16 v49, v51, v49, v33 neg_lo:[1,0,0] neg_hi:[1,0,0]
	v_mov_b32_e32 v236, 0
	v_cvt_pk_f16_f32 v50, v36, v37
	v_cvt_pk_f16_f32 v51, v38, v39
	v_and_b32 v34, s35, v50
	v_and_b32 v35, s35, v51
	v_pk_fma_f16 v32, v34, s42, v227
	v_pk_fma_f16 v33, v35, s42, v227
	v_pk_fma_f16 v32, v32, v34, s43
	v_pk_fma_f16 v33, v33, v35, s43
	s_nop 0
	v_pk_mul_f16 v32, v32, v34
	v_pk_mul_f16 v33, v33, v35
	v_exp_f16_sdwa v32, v32 dst_sel:WORD_0 dst_unused:UNUSED_PRESERVE src0_sel:WORD_0
	v_exp_f16_sdwa v33, v33 dst_sel:WORD_0 dst_unused:UNUSED_PRESERVE src0_sel:WORD_0
	v_exp_f16_sdwa v32, v32 dst_sel:WORD_1 dst_unused:UNUSED_PRESERVE src0_sel:WORD_1
	v_exp_f16_sdwa v33, v33 dst_sel:WORD_1 dst_unused:UNUSED_PRESERVE src0_sel:WORD_1
	v_pk_add_f16 v36, v50, v34
	v_pk_add_f16 v37, v51, v35
	v_pk_fma_f16 v32, v34, v32, v36 neg_lo:[1,0,0] neg_hi:[1,0,0]
	v_pk_fma_f16 v33, v35, v33, v37 neg_lo:[1,0,0] neg_hi:[1,0,0]
	s_nop 0
	v_cvt_pk_f16_f32 v38, v40, v41
	v_cvt_pk_f16_f32 v39, v42, v43
	v_and_b32 v36, s35, v38
	v_and_b32 v37, s35, v39
	v_pk_fma_f16 v34, v36, s42, v227
	v_pk_fma_f16 v35, v37, s42, v227
	v_pk_fma_f16 v34, v34, v36, s43
	v_pk_fma_f16 v35, v35, v37, s43
	s_nop 0
	v_pk_mul_f16 v34, v34, v36
	v_pk_mul_f16 v35, v35, v37
	v_exp_f16_sdwa v34, v34 dst_sel:WORD_0 dst_unused:UNUSED_PRESERVE src0_sel:WORD_0
	v_exp_f16_sdwa v35, v35 dst_sel:WORD_0 dst_unused:UNUSED_PRESERVE src0_sel:WORD_0
	v_exp_f16_sdwa v34, v34 dst_sel:WORD_1 dst_unused:UNUSED_PRESERVE src0_sel:WORD_1
	v_exp_f16_sdwa v35, v35 dst_sel:WORD_1 dst_unused:UNUSED_PRESERVE src0_sel:WORD_1
	v_pk_add_f16 v40, v38, v36
	v_pk_add_f16 v41, v39, v37
	v_pk_fma_f16 v34, v36, v34, v40 neg_lo:[1,0,0] neg_hi:[1,0,0]
	v_pk_fma_f16 v35, v37, v35, v41 neg_lo:[1,0,0] neg_hi:[1,0,0]
	s_nop 0
	v_cvt_pk_f16_f32 v40, v44, v45
	v_cvt_pk_f16_f32 v41, v46, v47
	v_and_b32 v38, s35, v40
	v_and_b32 v39, s35, v41
	v_pk_fma_f16 v36, v38, s42, v227
	v_pk_fma_f16 v37, v39, s42, v227
	v_pk_fma_f16 v36, v36, v38, s43
	v_pk_fma_f16 v37, v37, v39, s43
	s_nop 0
	v_pk_mul_f16 v36, v36, v38
	v_pk_mul_f16 v37, v37, v39
	v_exp_f16_sdwa v36, v36 dst_sel:WORD_0 dst_unused:UNUSED_PRESERVE src0_sel:WORD_0
	v_exp_f16_sdwa v37, v37 dst_sel:WORD_0 dst_unused:UNUSED_PRESERVE src0_sel:WORD_0
	v_exp_f16_sdwa v36, v36 dst_sel:WORD_1 dst_unused:UNUSED_PRESERVE src0_sel:WORD_1
	v_exp_f16_sdwa v37, v37 dst_sel:WORD_1 dst_unused:UNUSED_PRESERVE src0_sel:WORD_1
	v_pk_add_f16 v42, v40, v38
	v_pk_add_f16 v43, v41, v39
	v_pk_fma_f16 v36, v38, v36, v42 neg_lo:[1,0,0] neg_hi:[1,0,0]
	v_pk_fma_f16 v37, v39, v37, v43 neg_lo:[1,0,0] neg_hi:[1,0,0]
	s_nop 0
	v_cvt_pk_f16_f32 v42, v16, v17
	v_cvt_pk_f16_f32 v43, v18, v19
	v_and_b32 v40, s35, v42
	v_and_b32 v41, s35, v43
	v_pk_fma_f16 v38, v40, s42, v227
	v_pk_fma_f16 v39, v41, s42, v227
	v_pk_fma_f16 v38, v38, v40, s43
	v_pk_fma_f16 v39, v39, v41, s43
	s_nop 0
	v_pk_mul_f16 v38, v38, v40
	v_pk_mul_f16 v39, v39, v41
	v_exp_f16_sdwa v38, v38 dst_sel:WORD_0 dst_unused:UNUSED_PRESERVE src0_sel:WORD_0
	v_exp_f16_sdwa v39, v39 dst_sel:WORD_0 dst_unused:UNUSED_PRESERVE src0_sel:WORD_0
	v_exp_f16_sdwa v38, v38 dst_sel:WORD_1 dst_unused:UNUSED_PRESERVE src0_sel:WORD_1
	v_exp_f16_sdwa v39, v39 dst_sel:WORD_1 dst_unused:UNUSED_PRESERVE src0_sel:WORD_1
	v_pk_add_f16 v16, v42, v40
	v_pk_add_f16 v17, v43, v41
	v_pk_fma_f16 v38, v40, v38, v16 neg_lo:[1,0,0] neg_hi:[1,0,0]
	v_pk_fma_f16 v39, v41, v39, v17 neg_lo:[1,0,0] neg_hi:[1,0,0]
	s_nop 0
	v_cvt_pk_f16_f32 v40, v20, v21
	v_cvt_pk_f16_f32 v41, v22, v23
	v_and_b32 v18, s35, v40
	v_and_b32 v19, s35, v41
	v_pk_fma_f16 v16, v18, s42, v227
	v_pk_fma_f16 v17, v19, s42, v227
	v_pk_fma_f16 v16, v16, v18, s43
	v_pk_fma_f16 v17, v17, v19, s43
	s_nop 0
	v_pk_mul_f16 v16, v16, v18
	v_pk_mul_f16 v17, v17, v19
	v_exp_f16_sdwa v16, v16 dst_sel:WORD_0 dst_unused:UNUSED_PRESERVE src0_sel:WORD_0
	v_exp_f16_sdwa v17, v17 dst_sel:WORD_0 dst_unused:UNUSED_PRESERVE src0_sel:WORD_0
	v_exp_f16_sdwa v16, v16 dst_sel:WORD_1 dst_unused:UNUSED_PRESERVE src0_sel:WORD_1
	v_exp_f16_sdwa v17, v17 dst_sel:WORD_1 dst_unused:UNUSED_PRESERVE src0_sel:WORD_1
	v_pk_add_f16 v20, v40, v18
	v_pk_add_f16 v21, v41, v19
	v_pk_fma_f16 v16, v18, v16, v20 neg_lo:[1,0,0] neg_hi:[1,0,0]
	v_pk_fma_f16 v17, v19, v17, v21 neg_lo:[1,0,0] neg_hi:[1,0,0]
	s_nop 0
	v_cvt_pk_f16_f32 v22, v24, v25
	v_cvt_pk_f16_f32 v23, v26, v27
	v_and_b32 v20, s35, v22
	v_and_b32 v21, s35, v23
	v_pk_fma_f16 v18, v20, s42, v227
	v_pk_fma_f16 v19, v21, s42, v227
	v_pk_fma_f16 v18, v18, v20, s43
	v_pk_fma_f16 v19, v19, v21, s43
	s_nop 0
	v_pk_mul_f16 v18, v18, v20
	v_pk_mul_f16 v19, v19, v21
	v_exp_f16_sdwa v18, v18 dst_sel:WORD_0 dst_unused:UNUSED_PRESERVE src0_sel:WORD_0
	v_exp_f16_sdwa v19, v19 dst_sel:WORD_0 dst_unused:UNUSED_PRESERVE src0_sel:WORD_0
	v_exp_f16_sdwa v18, v18 dst_sel:WORD_1 dst_unused:UNUSED_PRESERVE src0_sel:WORD_1
	v_exp_f16_sdwa v19, v19 dst_sel:WORD_1 dst_unused:UNUSED_PRESERVE src0_sel:WORD_1
	v_pk_add_f16 v24, v22, v20
	v_pk_add_f16 v25, v23, v21
	v_pk_fma_f16 v18, v20, v18, v24 neg_lo:[1,0,0] neg_hi:[1,0,0]
	v_pk_fma_f16 v19, v21, v19, v25 neg_lo:[1,0,0] neg_hi:[1,0,0]
	s_nop 0
	v_cvt_pk_f16_f32 v24, v28, v29
	v_cvt_pk_f16_f32 v25, v30, v31
	v_and_b32 v22, s35, v24
	v_and_b32 v23, s35, v25
	v_pk_fma_f16 v20, v22, s42, v227
	v_pk_fma_f16 v21, v23, s42, v227
	v_pk_fma_f16 v20, v20, v22, s43
	v_pk_fma_f16 v21, v21, v23, s43
	s_nop 0
	v_pk_mul_f16 v20, v20, v22
	v_pk_mul_f16 v21, v21, v23
	v_exp_f16_sdwa v20, v20 dst_sel:WORD_0 dst_unused:UNUSED_PRESERVE src0_sel:WORD_0
	v_exp_f16_sdwa v21, v21 dst_sel:WORD_0 dst_unused:UNUSED_PRESERVE src0_sel:WORD_0
	v_exp_f16_sdwa v20, v20 dst_sel:WORD_1 dst_unused:UNUSED_PRESERVE src0_sel:WORD_1
	v_exp_f16_sdwa v21, v21 dst_sel:WORD_1 dst_unused:UNUSED_PRESERVE src0_sel:WORD_1
	v_pk_add_f16 v26, v24, v22
	v_pk_add_f16 v27, v25, v23
	v_pk_fma_f16 v20, v22, v20, v26 neg_lo:[1,0,0] neg_hi:[1,0,0]
	v_pk_fma_f16 v21, v23, v21, v27 neg_lo:[1,0,0] neg_hi:[1,0,0]
	ds_write2st64_b64 v234, v[48:49], v[38:39] offset0:3 offset1:4
	ds_write2st64_b64 v231, v[32:33], v[16:17] offset0:7 offset1:8
	ds_write2st64_b64 v232, v[34:35], v[18:19] offset0:11 offset1:12
	ds_write2st64_b64 v233, v[36:37], v[20:21] offset0:15 offset1:16
	v_mov_b64_e32 v[30:31], v[14:15]
	v_mov_b64_e32 v[28:29], v[12:13]
	v_mov_b64_e32 v[26:27], v[10:11]
	v_mov_b64_e32 v[24:25], v[8:9]
	v_mov_b64_e32 v[22:23], v[6:7]
	v_mov_b64_e32 v[20:21], v[4:5]
	v_mov_b64_e32 v[18:19], v[2:3]
	v_mov_b64_e32 v[16:17], v[0:1]
	s_waitcnt vmcnt(2)
	s_branch .LBB0_25

	.amdhsa_kernel _Z12local_kernelPKfPKDF16_S2_Pf5HeadPS3_
		.amdhsa_group_segment_fixed_size 162304
		.amdhsa_private_segment_fixed_size 0
		.amdhsa_kernarg_size 112
		.amdhsa_user_sgpr_count 2
		.amdhsa_user_sgpr_dispatch_ptr 0
		.amdhsa_user_sgpr_queue_ptr 0
		.amdhsa_user_sgpr_kernarg_segment_ptr 1
		.amdhsa_user_sgpr_dispatch_id 0
		.amdhsa_user_sgpr_kernarg_preload_length 0
		.amdhsa_user_sgpr_kernarg_preload_offset 0
		.amdhsa_user_sgpr_private_segment_size 0
		.amdhsa_uses_dynamic_stack 0
		.amdhsa_enable_private_segment 0
		.amdhsa_system_sgpr_workgroup_id_x 1
		.amdhsa_system_sgpr_workgroup_id_y 0
		.amdhsa_system_sgpr_workgroup_id_z 0
		.amdhsa_system_sgpr_workgroup_info 0
		.amdhsa_system_vgpr_workitem_id 0
		.amdhsa_next_free_vgpr 256
		.amdhsa_next_free_sgpr 96
		.amdhsa_accum_offset 256
		.amdhsa_reserve_vcc 1
		.amdhsa_float_round_mode_32 0
		.amdhsa_float_round_mode_16_64 0
		.amdhsa_float_denorm_mode_32 3
		.amdhsa_float_denorm_mode_16_64 3
		.amdhsa_dx10_clamp 1
		.amdhsa_ieee_mode 1
		.amdhsa_fp16_overflow 0
		.amdhsa_tg_split 0
		.amdhsa_exception_fp_ieee_invalid_op 0
		.amdhsa_exception_fp_denorm_src 0
		.amdhsa_exception_fp_ieee_div_zero 0
		.amdhsa_exception_fp_ieee_overflow 0
		.amdhsa_exception_fp_ieee_underflow 0
		.amdhsa_exception_fp_ieee_inexact 0
		.amdhsa_exception_int_div_zero 0
	.end_amdhsa_kernel

amdhsa.kernels:
  - .agpr_count:     0
    .args:
      - .actual_access:  read_only
        .address_space:  global
        .offset:         0
        .size:           8
        .value_kind:     global_buffer
      - .actual_access:  read_only
        .address_space:  global
        .offset:         8
        .size:           8
        .value_kind:     global_buffer
      - .actual_access:  read_only
        .address_space:  global
        .offset:         16
        .size:           8
        .value_kind:     global_buffer
      - .address_space:  global
        .offset:         24
        .size:           8
        .value_kind:     global_buffer
      - .offset:         32
        .size:           72
        .value_kind:     by_value
      - .address_space:  global
        .offset:         104
        .size:           8
        .value_kind:     global_buffer
    .group_segment_fixed_size: 162304
    .kernarg_segment_align: 8
    .kernarg_segment_size: 112
    .language:       OpenCL C
    .language_version:
      - 2
      - 0
    .max_flat_workgroup_size: 512
    .name:           _Z12local_kernelPKfPKDF16_S2_Pf5HeadPS3_
    .private_segment_fixed_size: 0
    .sgpr_count:     50
    .sgpr_spill_count: 0
    .symbol:         _Z12local_kernelPKfPKDF16_S2_Pf5HeadPS3_.kd
    .uniform_work_group_size: 1
    .uses_dynamic_stack: false
    .vgpr_count:     256
    .vgpr_spill_count: 0
    .wavefront_size: 64
  - .agpr_count:     0
    .args:
      - .actual_access:  read_only
        .address_space:  global
        .offset:         0
        .size:           8
        .value_kind:     global_buffer
      - .actual_access:  read_only
        .address_space:  global
        .offset:         8
        .size:           8
        .value_kind:     global_buffer
      - .actual_access:  write_only
        .address_space:  global
        .offset:         16
        .size:           8
        .value_kind:     global_buffer
      - .actual_access:  read_only
        .address_space:  global
        .offset:         24
        .size:           8
        .value_kind:     global_buffer
      - .actual_access:  read_only
        .address_space:  global
        .offset:         32
        .size:           8
        .value_kind:     global_buffer
      - .actual_access:  read_only
        .address_space:  global
        .offset:         40
        .size:           8
        .value_kind:     global_buffer
      - .actual_access:  read_only
        .address_space:  global
        .offset:         48
        .size:           8
        .value_kind:     global_buffer
      - .actual_access:  write_only
        .address_space:  global
        .offset:         56
        .size:           8
        .value_kind:     global_buffer
      - .actual_access:  write_only
        .address_space:  global
        .offset:         64
        .size:           8
        .value_kind:     global_buffer
      - .actual_access:  read_only
        .address_space:  global
        .offset:         72
        .size:           8
        .value_kind:     global_buffer
      - .actual_access:  read_only
        .address_space:  global
        .offset:         80
        .size:           8
        .value_kind:     global_buffer
    .group_segment_fixed_size: 162304
    .kernarg_segment_align: 8
    .kernarg_segment_size: 88
    .language:       OpenCL C
    .language_version:
      - 2
      - 0
    .max_flat_workgroup_size: 1024
    .name:           _Z19trunk_global_kernelPKfPKDF16_PDF16_S0_S2_S0_S0_PfS4_S0_S0_
    .private_segment_fixed_size: 0
    .sgpr_count:     48
    .sgpr_spill_count: 0
    .symbol:         _Z19trunk_global_kernelPKfPKDF16_PDF16_S0_S2_S0_S0_PfS4_S0_S0_.kd
    .uniform_work_group_size: 1
    .uses_dynamic_stack: false
    .vgpr_count:     103
    .vgpr_spill_count: 0
    .wavefront_size: 64
  - .agpr_count:     0
    .args:
      - .offset:         0
        .size:           96
        .value_kind:     by_value
      - .offset:         96
        .size:           96
        .value_kind:     by_value
      - .offset:         192
        .size:           176
        .value_kind:     by_value
      - .actual_access:  read_only
        .address_space:  global
        .offset:         368
        .size:           8
        .value_kind:     global_buffer
      - .actual_access:  read_only
        .address_space:  global
        .offset:         376
        .size:           8
        .value_kind:     global_buffer
      - .actual_access:  write_only
        .address_space:  global
        .offset:         384
        .size:           8
        .value_kind:     global_buffer
      - .actual_access:  write_only
        .address_space:  global
        .offset:         392
        .size:           8
        .value_kind:     global_buffer
      - .actual_access:  write_only
        .address_space:  global
        .offset:         400
        .size:           8
        .value_kind:     global_buffer
    .group_segment_fixed_size: 0
    .kernarg_segment_align: 8
    .kernarg_segment_size: 408
    .language:       OpenCL C
    .language_version:
      - 2
      - 0
    .max_flat_workgroup_size: 256
    .name:           _Z15prep_all_kernel5PrepPS_6HPrepPPKfS2_PDF16_S3_S3_
    .private_segment_fixed_size: 0
    .sgpr_count:     74
    .sgpr_spill_count: 0
    .symbol:         _Z15prep_all_kernel5PrepPS_6HPrepPPKfS2_PDF16_S3_S3_.kd
    .uniform_work_group_size: 1
    .uses_dynamic_stack: false
    .vgpr_count:     37
    .vgpr_spill_count: 0
    .wavefront_size: 64
